# baseline (speedup 1.0000x reference)
.Lmk_p72:
	v_lshlrev_b32_e32 v109, 2, v114
	v_bfe_u32 v121, v121, 16, 4
	v_mov_b64_e32 v[130:131], 0
	v_mov_b64_e32 v[132:133], 0
	v_mov_b64_e32 v[134:135], 0
	v_mov_b64_e32 v[136:137], 0
	v_mov_b64_e32 v[138:139], 0
	v_mov_b64_e32 v[140:141], 0
	v_mov_b64_e32 v[142:143], 0
	v_mov_b64_e32 v[144:145], 0
	v_and_b32_e32 v200, 1, v114
	v_cmp_eq_u32_e32 vcc, 1, v200
	s_nop 1
	v_cndmask_b32_e32 v124, v124, v174, vcc
	v_mov_b64_e32 v[168:169], s[12:13]
	v_mov_b64_e32 v[170:171], s[12:13]
	v_xor_b32_e32 v117, 64, v122
	s_mov_b32 s30, s85
	s_lshl_b32 s6, s43, 6
	s_sub_i32 s83, s44, s6
	s_lshl_b32 s6, s43, 8
	s_add_i32 s82, s78, s6
	s_mov_b32 s66, s41
	s_branch .LBB2_62

.LBB2_76:
	s_and_b64 vcc, exec, s[54:55]
	s_cbranch_vccz .LBB2_110
	s_cmp_gt_i32 s50, 35
	s_cbranch_scc1 .LBB2_110
	s_add_i32 s36, s50, 2
	s_mul_hi_i32 s0, s36, 0x55555556
	s_lshr_b32 s1, s0, 31
	s_add_i32 s0, s0, s1
	s_mul_i32 s0, s0, 3
	s_sub_i32 s37, s36, s0
	s_mulk_i32 s37, 0xc00
	s_add_i32 s38, s40, s37
	v_lshl_add_u32 v36, v114, 2, v129
	s_and_saveexec_b64 s[0:1], s[4:5]
	v_lshl_add_u32 v37, v110, 2, s38
	ds_write_b32 v37, v194
	s_or_b64 exec, exec, s[0:1]
	v_lshl_add_u32 v37, v36, 2, s38
	v_sub_u32_e32 v36, v125, v109
	s_waitcnt vmcnt(8)
	v_cmp_lt_i32_e32 vcc, 0, v36
	s_and_saveexec_b64 s[0:1], vcc
	ds_write_b32 v37, v164 offset:64
	s_or_b64 exec, exec, s[0:1]
	v_cmp_lt_i32_e32 vcc, 1, v36
	s_and_saveexec_b64 s[0:1], vcc
	ds_write_b32 v37, v165 offset:68
	s_or_b64 exec, exec, s[0:1]
	v_cmp_lt_i32_e32 vcc, 2, v36
	s_and_saveexec_b64 s[0:1], vcc
	ds_write_b32 v37, v166 offset:72
	s_or_b64 exec, exec, s[0:1]
	v_cmp_lt_i32_e32 vcc, 3, v36
	s_and_saveexec_b64 s[0:1], vcc
	ds_write_b32 v37, v167 offset:76
	s_or_b64 exec, exec, s[0:1]
	v_add_u32_e32 v36, v129, v114
	v_cmp_lt_i32_e32 vcc, v119, v125
	s_and_saveexec_b64 s[0:1], vcc
	s_cbranch_execz .LBB2_109
	s_add_i32 s37, s47, s37
	v_lshl_add_u32 v130, v36, 2, s37
	v_lshlrev_b32_e32 v36, 2, v120
	v_mov_b32_e32 v37, 0
	v_mad_i64_i32 v[36:37], s[36:37], s36, v116, v[36:37]
	v_lshl_add_u64 v[36:37], v[0:1], 0, v[36:37]
	s_mov_b64 s[36:37], 0
	v_mov_b32_e32 v34, v119
	s_branch .LBB2_91

.Lmk_max:
	v_cndmask_b32_e64 v161, v185, v34, s[56:57]
	s_nop 1
	v_max_f32_dpp v161, v161, v161 row_shr:1 row_mask:0xf bank_mask:0xf
	v_bfe_u32 v121, v183, 16, 4
	s_nop 0
	v_max_f32_dpp v161, v161, v161 row_shr:2 row_mask:0xf bank_mask:0xf
	v_add_u32_e32 v229, s82, v172
	v_add_u32_e32 v230, s82, v173
	v_max_f32_dpp v161, v161, v161 row_shr:4 row_mask:0xf bank_mask:0xf
	ds_read_u16 v224, v229 offset:0
	ds_read_u16 v225, v229 offset:32
	v_max_f32_dpp v161, v161, v161 row_shr:8 row_mask:0xf bank_mask:0xf
	ds_read_u16 v226, v229 offset:64
	ds_read_u16 v227, v229 offset:96
	v_max_f32_dpp v161, v161, v161 row_bcast:15 row_mask:0xa bank_mask:0xf
	ds_read_u16 v232, v229 offset:128
	ds_read_u16 v233, v229 offset:160
	v_max_f32_dpp v161, v161, v161 row_bcast:31 row_mask:0xc bank_mask:0xf
	ds_read_u16 v234, v229 offset:192
	ds_read_u16 v235, v229 offset:224
	v_readlane_b32 s70, v161, 63
	ds_read_b32 v183, v230
	s_and_b64 vcc, exec, s[54:55]
	s_cbranch_vccz .Lmk_rescale
.Lmk_norescale:
	v_mov_b32_e32 v195, s70
	v_add_f32_e32 v184, 0x40200000, v195
	s_branch .Lmk_nomax
.Lmk_rescale:
	v_subrev_f32_e32 v162, s70, v195
	v_mul_f32_e32 v162, 0x3fb8aa3b, v162
	v_exp_f32_e32 v248, v162
	s_nop 0
	v_pk_mul_f32 v[56:57], v[248:249], v[56:57] op_sel_hi:[0,1]
	v_pk_mul_f32 v[54:55], v[248:249], v[54:55] op_sel_hi:[0,1]
	v_pk_mul_f32 v[60:61], v[248:249], v[60:61] op_sel_hi:[0,1]
	v_pk_mul_f32 v[58:59], v[248:249], v[58:59] op_sel_hi:[0,1]
	v_pk_mul_f32 v[64:65], v[248:249], v[64:65] op_sel_hi:[0,1]
	v_pk_mul_f32 v[62:63], v[248:249], v[62:63] op_sel_hi:[0,1]
	v_pk_mul_f32 v[68:69], v[248:249], v[68:69] op_sel_hi:[0,1]
	v_pk_mul_f32 v[66:67], v[248:249], v[66:67] op_sel_hi:[0,1]
	v_pk_mul_f32 v[72:73], v[72:73], v[248:249] op_sel_hi:[1,0]
	v_pk_mul_f32 v[70:71], v[70:71], v[248:249] op_sel_hi:[1,0]
	s_branch .Lmk_norescale

.Lmk_nolist:
	v_mov_b32_e32 v125, 0
	s_branch .LBB2_103

.LBB2_93:
	v_mov_b32_e32 v184, v185
	s_lshl_b32 s0, s50, 7
	s_add_i32 s0, s0, 0x26000
	v_lshl_add_u32 v36, v107, 4, s0
	ds_read_b128 v[240:243], v36
	ds_read_b128 v[244:247], v36 offset:64
	s_cmp_gt_i32 s50, 35
	s_cbranch_scc1 .Lmk_nolist
	v_mov_b32_dpp v174, v124 quad_perm:[1,1,1,1] row_mask:0xf bank_mask:0xf
	v_mov_b32_dpp v124, v124 quad_perm:[0,0,0,0] row_mask:0xf bank_mask:0xf
	v_sub_u32_e32 v125, v174, v124
	s_add_i32 s0, s50, 2
	v_cndmask_b32_e64 v34, 0, v125, s[2:3]
	s_mul_i32 s0, s0, 0xc3500
	v_lshl_add_u32 v36, v124, 2, v118
	v_add_u32_dpp v34, v34, v34 row_shr:1 row_mask:0xf bank_mask:0xf bound_ctrl:1
	s_add_u32 s0, s90, s0
	s_addc_u32 s1, s91, 0
	v_add_u32_dpp v34, v34, v34 row_shr:2 row_mask:0xf bank_mask:0xf bound_ctrl:1
	v_mov_b32_e32 v120, v124
	s_nop 0
	v_add_u32_dpp v34, v34, v34 row_shr:4 row_mask:0xf bank_mask:0xf bound_ctrl:1
	global_load_dwordx4 v[164:167], v36, s[0:1]
	s_nop 0
	v_add_u32_dpp v34, v34, v34 row_shr:8 row_mask:0xf bank_mask:0xf bound_ctrl:1
	s_nop 1
	v_add_u32_dpp v34, v34, v34 row_bcast:15 row_mask:0xa bank_mask:0xf
	s_nop 1
	v_add_u32_dpp v34, v34, v34 row_bcast:31 row_mask:0xc bank_mask:0xf
	v_sub_u32_e32 v129, v34, v125
	v_sub_u32_e32 v36, 0x2f0, v129
	v_min_i32_e32 v125, v125, v36
